# hoisted four-waves-per-row version whose gatherer reads the three other scanners' flags with one batched LDS read instead of three sequential poll loops
# baseline (speedup 1.0000x reference)
.Lg_pollall:
	ds_read_b32 v1, v7
	ds_read_b32 v2, v7 offset:16
	ds_read_b32 v13, v7 offset:32
	s_waitcnt lgkmcnt(0)
	v_readfirstlane_b32 s4, v1
	v_readfirstlane_b32 s16, v2
	v_readfirstlane_b32 s17, v13
	s_cmp_eq_u32 s4, 0
	s_cbranch_scc1 .Lg_again
	s_cmp_eq_u32 s16, 0
	s_cbranch_scc1 .Lg_again
	s_cmp_lg_u32 s17, 0
	s_cbranch_scc1 .Lg_gotall
.Lg_again:
	s_sub_u32 s19, s19, 1
	s_cmp_eq_u32 s19, 0
	s_cbranch_scc1 .Lg_gotall
	s_sleep 1
	s_branch .Lg_pollall
